# sel tile: rare causal-mask and rescale blocks moved out of line so the common path falls through; group-1 PV block placed after its check
# speedup vs baseline: 1.0468x; 1.0022x over previous
; #define LAS __attribute__((address_space(3)))
; __device__ __forceinline__ unsigned lds_addr(const LAS void* p) { return (unsigned)(size_t)p; }
; template <bool DUMMY> __device__ __forceinline__ void sel_phase(Frame& F) {
;     ...
; #pragma unroll 1
;             for (int h = 0; h < 3; ++h) {
;                 if (h > 0 && ((cj >> (23 + h)) & 1u) == 0u) continue;
;                 const int jc = (int)((cj >> (8 * h)) & 0xffu);
;                 LAS unsigned char* sb = F.lds + (((p & 1) * 3) + h) * SLOTS;
;                 unsigned byte = (cb >> (8 * h)) & 0xffu;
;                 if (DUMMY && MK_EXP == 1) byte = 0u;
;                 const unsigned a0 = byte & 0xfu, a1 = byte >> 4;
;                 if (byte == 0u) continue;
;                 const bool selA = ((a0 >> (c >> 2)) & 1u) != 0u, selB = ((a1 >> (c >> 2)) & 1u) != 0u;
;                 const float NINF = -__builtin_inff();
;                 const int kb = jc * 64; const bool diag = (jc == cur); f32x4 s0[4], s1[4];
;                 const float bA = selA ? 0.f : NINF, bB = selB ? 0.f : NINF;
;                 if (a0 != 0u) {
;                     const float rf = sm8_ref(g0);
;                     VT8Frag vf; qk8_tile_c(s0, g0, lds_addr(sb) + (unsigned)klane, bA + (5.f - rf)); pv8_issue(vf, lds_addr(sb + K8TB) + (unsigned)vtlane);
;                     if (diag) mask_scores(s0, tokA, 0x40000000u, kb, kq);
;                     online_sm8(s0, g0, rf);
;                     pv8_mm(g0, s0, vf);
;                 }
;                 if (a1 != 0u) {
;                     const float rf = sm8_ref(g1);
;                     VT8Frag vf; qk8_tile_c(s0, g1, lds_addr(sb) + (unsigned)klane, bB + (5.f - rf)); pv8_issue(vf, lds_addr(sb + K8TB) + (unsigned)vtlane);
;                     if (diag) mask_scores(s0, tokA + 4, 0x40000000u, kb, kq);
;                     online_sm8(s0, g1, rf);
;                     pv8_mm(g1, s0, vf);
;                 }
;             }
;             cj = nj; cb = nb;
.LBB0_1796:
	s_bitcmp1_b32 s36, 0
	s_cselect_b32 s12, 0xe400, 0
	s_mov_b32 s36, 0
	v_add_u32_e32 v207, s12, v173
	v_add_u32_e32 v208, s12, v174
	s_mov_b32 s37, 0
	s_branch .LBB0_1799
.LBB0_1798:
	s_add_i32 s37, s37, 1
	s_add_i32 s36, s36, 8
	v_add_u32_e32 v207, 0x4c00, v207
	s_cmp_eq_u32 s37, 3
	v_add_u32_e32 v208, 0x4c00, v208
	s_cbranch_scc1 .LBB0_1814

; __device__ __forceinline__ float xmax16(float v) { float a = v, b = v; PL_SWAP16(a, b); return fmaxf(a, b); }
; __device__ __forceinline__ float xmax32(float v) { float a = v, b = v; PL_SWAP32(a, b); return fmaxf(a, b); }
; __device__ __forceinline__ unsigned lds_addr(const LAS void* p) { return (unsigned)(size_t)p; }
; template <class G> __device__ __forceinline__ void online_sm8(f32x4 (&s)[4], G& g, const float ref) {
;     float mx = s[0][0];
; #pragma unroll
;     for (int T_ = 0; T_ < 4; ++T_)
; #pragma unroll
;         for (int i = 0; i < 4; ++i) mx = fmaxf(mx, s[T_][i]);
;     const float t = mx + (ref - 5.f);
;     if (!__all(t <= g.m + SM_THR8)) {
;         const float mr = xmax32(xmax16(t));
;         const float mn = fmaxf(g.m, mr); const float al = __builtin_amdgcn_exp2f(g.m - mn); g.m = mn; g.l *= al;
; template <bool DUMMY> __device__ __forceinline__ void sel_phase(Frame& F) {
;     ...
;                 if (a0 != 0u) {
;                     const float rf = sm8_ref(g0);
;                     VT8Frag vf; qk8_tile_c(s0, g0, lds_addr(sb) + (unsigned)klane, bA + (5.f - rf)); pv8_issue(vf, lds_addr(sb + K8TB) + (unsigned)vtlane);
;                     if (diag) mask_scores(s0, tokA, 0x40000000u, kb, kq);
;                     online_sm8(s0, g0, rf);
;                     pv8_mm(g0, s0, vf);
.Lsel_nodma:
	s_lshr_b32 s45, s67, s36
	s_and_b32 s97, s45, 0xff
	s_cbranch_scc0 .LBB0_1798
	ds_read_b128 v[84:87], v208 offset:0
	ds_read_b128 v[88:91], v208 offset:16
	ds_read_b128 v[92:95], v208 offset:0x900
	ds_read_b128 v[96:99], v208 offset:0x910
	ds_read_b128 v[118:121], v208 offset:0x1200
	ds_read_b128 v[122:125], v208 offset:0x1210
	s_and_b32 vcc_lo, s45, 15
	s_cbranch_scc0 .Lsel_g1_pre
	v_and_b32_e32 v18, s45, v154
	v_cmp_eq_u32_e32 vcc, 0, v18
	s_lshr_b32 s44, s66, s36
	s_and_b32 s44, s44, 0xff
	v_cndmask_b32_e32 v210, v216, v181, vcc
	v_mov_b32_e32 v211, v210
	v_mov_b32_e32 v212, v210
	v_mov_b32_e32 v213, v210
	ds_read_b128 v[126:129], v208 offset:0x1b00
	ds_read_b128 v[130:133], v208 offset:0x1b10
	s_waitcnt lgkmcnt(6)
	v_mfma_scale_f32_16x16x128_f8f6f4 v[84:87], v[84:91], v[0:7], v[210:213], v178, v177 op_sel_hi:[0,0,0]
	ds_read_b64 v[148:149], v207 offset:0
	ds_read_b64 v[146:147], v207 offset:32
	ds_read_b64 v[144:145], v207 offset:0x500
	ds_read_b64 v[142:143], v207 offset:0x520
	ds_read_b64 v[140:141], v207 offset:0xa00
	ds_read_b64 v[136:137], v207 offset:0xa20
	ds_read_b64 v[138:139], v207 offset:0xf00
	ds_read_b64 v[134:135], v207 offset:0xf20
	s_waitcnt lgkmcnt(12)
	v_mfma_scale_f32_16x16x128_f8f6f4 v[88:91], v[92:99], v[0:7], v[210:213], v178, v177 op_sel_hi:[0,0,0]
	s_waitcnt lgkmcnt(10)
	v_mfma_scale_f32_16x16x128_f8f6f4 v[92:95], v[118:125], v[0:7], v[210:213], v178, v177 op_sel_hi:[0,0,0]
	s_waitcnt lgkmcnt(8)
	v_mfma_scale_f32_16x16x128_f8f6f4 v[96:99], v[126:133], v[0:7], v[210:213], v178, v177 op_sel_hi:[0,0,0]
	ds_read_b64 v[132:133], v207 offset:0x1400
	ds_read_b64 v[130:131], v207 offset:0x1420
	ds_read_b64 v[128:129], v207 offset:0x1900
	ds_read_b64 v[126:127], v207 offset:0x1920
	ds_read_b64 v[124:125], v207 offset:0x1e00
	ds_read_b64 v[120:121], v207 offset:0x1e20
	ds_read_b64 v[118:119], v207 offset:0x2300
	ds_read_b64 v[122:123], v207 offset:0x2320
	s_cmp_eq_u32 s44, s58
	s_cbranch_scc1 .Lsel_diag_g0
.LBB0_1806:
	v_max_f32_e32 v18, v84, v85
	v_max3_f32 v18, v18, v86, v87
	v_max3_f32 v18, v18, v88, v89
	v_max3_f32 v18, v18, v90, v91
	v_max3_f32 v18, v18, v92, v93
	v_max3_f32 v18, v18, v94, v95
	v_max3_f32 v18, v18, v96, v97
	v_max3_f32 v114, v18, v98, v99
	v_add_f32_e32 v150, v217, v114
	v_cmp_le_f32_e32 vcc, v150, v218
	s_cmp_eq_u64 vcc, exec
	s_cbranch_scc0 .Lsel_resc_g0

; __device__ __forceinline__ unsigned pk4_fp8(float a, float b, float c, float d) { unsigned w = 0u; w = __builtin_amdgcn_cvt_pk_fp8_f32(a, b, w, false); w = __builtin_amdgcn_cvt_pk_fp8_f32(c, d, w, true); return w; }
; __device__ __forceinline__ unsigned lds_addr(const LAS void* p) { return (unsigned)(size_t)p; }
; #define LGKM_W(n) asm volatile("s_waitcnt lgkmcnt(" #n ")" ::: "memory"); SBAR()
; #define PV8_MM(dt) do { g.o[dt] = __builtin_amdgcn_mfma_f32_16x16x32_fp8_fp8(f.a[dt][0], b0, g.o[dt], 0, 0, 0); g.o[dt] = __builtin_amdgcn_mfma_f32_16x16x32_fp8_fp8(f.a[dt][1], b1, g.o[dt], 0, 0, 0); } while (0)
; template <class G> __device__ __forceinline__ void pv8_mm(G& g, const f32x4 (&s)[4], const VT8Frag& f) {
;     ...
;     unsigned pa[4];
; #pragma unroll
;     for (int T_ = 0; T_ < 4; ++T_) pa[T_] = pk4_fp8(s[T_][0], s[T_][1], s[T_][2], s[T_][3]);
;     const long b0 = (long)(((unsigned long long)pa[1] << 32) | pa[0]), b1 = (long)(((unsigned long long)pa[3] << 32) | pa[2]);
;     LGKM_W(14); PV8_MM(0); LGKM_W(12); PV8_MM(1); LGKM_W(10); PV8_MM(2); LGKM_W(8); PV8_MM(3);
;     LGKM_W(6); PV8_MM(4); LGKM_W(4); PV8_MM(5); LGKM_W(2); PV8_MM(6); LGKM_W(0); PV8_MM(7);
;     ...
; }
; template <bool DUMMY> __device__ __forceinline__ void sel_phase(Frame& F) {
;     ...
;                 if (a1 != 0u) {
;                     const float rf = sm8_ref(g1);
;                     VT8Frag vf; qk8_tile_c(s0, g1, lds_addr(sb) + (unsigned)klane, bB + (5.f - rf)); pv8_issue(vf, lds_addr(sb + K8TB) + (unsigned)vtlane);
;                     if (diag) mask_scores(s0, tokA + 4, 0x40000000u, kb, kq);
;                     online_sm8(s0, g1, rf);
;                     pv8_mm(g1, s0, vf);
;                 }
.Lsel_g1_pre:
	s_lshr_b32 s45, s45, 4
	v_and_b32_e32 v18, s45, v154
	v_cmp_eq_u32_e32 vcc, 0, v18
	s_lshr_b32 s44, s66, s36
	s_and_b32 s44, s44, 0xff
	v_cndmask_b32_e32 v210, v220, v181, vcc
	v_mov_b32_e32 v211, v210
	v_mov_b32_e32 v212, v210
	v_mov_b32_e32 v213, v210
	ds_read_b128 v[126:129], v208 offset:0x1b00
	ds_read_b128 v[130:133], v208 offset:0x1b10
	s_waitcnt lgkmcnt(6)
	v_mfma_scale_f32_16x16x128_f8f6f4 v[84:87], v[84:91], v[8:15], v[210:213], v178, v177 op_sel_hi:[0,0,0]
	ds_read_b64 v[148:149], v207 offset:0
	ds_read_b64 v[146:147], v207 offset:32
	ds_read_b64 v[144:145], v207 offset:0x500
	ds_read_b64 v[142:143], v207 offset:0x520
	ds_read_b64 v[140:141], v207 offset:0xa00
	ds_read_b64 v[136:137], v207 offset:0xa20
	ds_read_b64 v[138:139], v207 offset:0xf00
	ds_read_b64 v[134:135], v207 offset:0xf20
	s_waitcnt lgkmcnt(12)
	v_mfma_scale_f32_16x16x128_f8f6f4 v[88:91], v[92:99], v[8:15], v[210:213], v178, v177 op_sel_hi:[0,0,0]
	s_waitcnt lgkmcnt(10)
	v_mfma_scale_f32_16x16x128_f8f6f4 v[92:95], v[118:125], v[8:15], v[210:213], v178, v177 op_sel_hi:[0,0,0]
	s_waitcnt lgkmcnt(8)
	v_mfma_scale_f32_16x16x128_f8f6f4 v[96:99], v[126:133], v[8:15], v[210:213], v178, v177 op_sel_hi:[0,0,0]
	ds_read_b64 v[132:133], v207 offset:0x1400
	ds_read_b64 v[130:131], v207 offset:0x1420
	ds_read_b64 v[128:129], v207 offset:0x1900
	ds_read_b64 v[126:127], v207 offset:0x1920
	ds_read_b64 v[124:125], v207 offset:0x1e00
	ds_read_b64 v[120:121], v207 offset:0x1e20
	ds_read_b64 v[118:119], v207 offset:0x2300
	ds_read_b64 v[122:123], v207 offset:0x2320
	s_cmp_eq_u32 s44, s58
	s_cbranch_scc1 .Lsel_diag_g1
.LBB0_1812:
	v_max_f32_e32 v114, v84, v85
	v_max3_f32 v114, v114, v86, v87
	v_max3_f32 v114, v114, v88, v89
	v_max3_f32 v114, v114, v90, v91
	v_max3_f32 v114, v114, v92, v93
	v_max3_f32 v114, v114, v94, v95
	v_max3_f32 v114, v114, v96, v97
	v_max3_f32 v114, v114, v98, v99
	v_add_f32_e32 v150, v221, v114
	v_cmp_le_f32_e32 vcc, v150, v222
	s_cmp_eq_u64 vcc, exec
	s_cbranch_scc0 .Lsel_resc_g1
.LBB0_1797:
	v_exp_f32_e32 v240, v84
	v_exp_f32_e32 v241, v85
	v_exp_f32_e32 v242, v86
	v_exp_f32_e32 v243, v87
	v_exp_f32_e32 v244, v88
	v_exp_f32_e32 v245, v89
	v_exp_f32_e32 v246, v90
	v_exp_f32_e32 v247, v91
	s_waitcnt lgkmcnt(0)
	v_cvt_pk_fp8_f32 v84, v240, v241
	v_cvt_pk_fp8_f32 v85, v244, v245
	v_cvt_pk_fp8_f32 v84, v242, v243 op_sel:[0,0,1]
	v_cvt_pk_fp8_f32 v85, v246, v247 op_sel:[0,0,1]
	v_exp_f32_e32 v248, v92
	v_exp_f32_e32 v249, v93
	v_mfma_f32_16x16x32_fp8_fp8 v[48:51], v[148:149], v[84:85], v[48:51]
	v_exp_f32_e32 v250, v94
	v_mfma_f32_16x16x32_fp8_fp8 v[44:47], v[144:145], v[84:85], v[44:47]
	v_exp_f32_e32 v251, v95
	v_mfma_f32_16x16x32_fp8_fp8 v[40:43], v[140:141], v[84:85], v[40:43]
	v_exp_f32_e32 v252, v96
	v_mfma_f32_16x16x32_fp8_fp8 v[36:39], v[138:139], v[84:85], v[36:39]
	v_exp_f32_e32 v253, v97
	v_mfma_f32_16x16x32_fp8_fp8 v[32:35], v[132:133], v[84:85], v[32:35]
	v_exp_f32_e32 v254, v98
	v_mfma_f32_16x16x32_fp8_fp8 v[28:31], v[128:129], v[84:85], v[28:31]
	v_exp_f32_e32 v255, v99
	v_mfma_f32_16x16x32_fp8_fp8 v[24:27], v[124:125], v[84:85], v[24:27]
	v_mfma_f32_16x16x32_fp8_fp8 v[20:23], v[118:119], v[84:85], v[20:23]
	v_cvt_pk_fp8_f32 v86, v248, v249
	v_cvt_pk_fp8_f32 v87, v252, v253
	v_cvt_pk_fp8_f32 v86, v250, v251 op_sel:[0,0,1]
	v_cvt_pk_fp8_f32 v87, v254, v255 op_sel:[0,0,1]
	v_add_f32_e32 v240, v240, v241
	v_add_f32_e32 v242, v242, v243
	v_mfma_f32_16x16x32_fp8_fp8 v[48:51], v[146:147], v[86:87], v[48:51]
	v_add_f32_e32 v244, v244, v245
	v_add_f32_e32 v246, v246, v247
	v_mfma_f32_16x16x32_fp8_fp8 v[44:47], v[142:143], v[86:87], v[44:47]
	v_add_f32_e32 v248, v248, v249
	v_add_f32_e32 v250, v250, v251
	v_mfma_f32_16x16x32_fp8_fp8 v[40:43], v[136:137], v[86:87], v[40:43]
	v_add_f32_e32 v252, v252, v253
	v_add_f32_e32 v254, v254, v255
	v_mfma_f32_16x16x32_fp8_fp8 v[36:39], v[134:135], v[86:87], v[36:39]
	v_add_f32_e32 v240, v240, v242
	v_add_f32_e32 v244, v244, v246
	v_mfma_f32_16x16x32_fp8_fp8 v[32:35], v[130:131], v[86:87], v[32:35]
	v_add_f32_e32 v248, v248, v250
	v_add_f32_e32 v252, v252, v254
	v_mfma_f32_16x16x32_fp8_fp8 v[28:31], v[126:127], v[86:87], v[28:31]
	v_add_f32_e32 v240, v240, v244
	v_add_f32_e32 v248, v248, v252
	v_mfma_f32_16x16x32_fp8_fp8 v[24:27], v[120:121], v[86:87], v[24:27]
	v_add_f32_e32 v240, v240, v248
	v_add_f32_e32 v182, v182, v240
	v_mfma_f32_16x16x32_fp8_fp8 v[20:23], v[122:123], v[86:87], v[20:23]
	s_branch .LBB0_1798
.Lsel_diag_g0:
	s_lshl_b32 s12, s44, 6
	v_add_u32_e32 v18, s12, v155
	v_sub_u32_e32 v114, s55, v18
	v_cmp_gt_u32_e32 vcc, 2.0, v114
	v_sub_u32_e32 v114, v18, v16
	s_nop 2
	v_cndmask_b32_e32 v84, v181, v84, vcc
	v_cmp_lt_u32_e32 vcc, s91, v114
	v_sub_u32_e32 v114, v184, v18
	s_nop 0
	v_cndmask_b32_e32 v85, v181, v85, vcc
	v_cmp_gt_u32_e32 vcc, 2.0, v114
	v_sub_u32_e32 v114, v185, v18
	s_nop 0
	v_cndmask_b32_e32 v86, v181, v86, vcc
	v_cmp_gt_u32_e32 vcc, 2.0, v114
	v_sub_u32_e32 v114, s68, v18
	s_nop 0
	v_cndmask_b32_e32 v87, v181, v87, vcc
	v_cmp_gt_u32_e32 vcc, 2.0, v114
	v_sub_u32_e32 v114, v186, v18
	s_nop 0
	v_cndmask_b32_e32 v88, v181, v88, vcc
	v_cmp_gt_u32_e32 vcc, 2.0, v114
	v_sub_u32_e32 v114, v187, v18
	s_nop 0
	v_cndmask_b32_e32 v89, v181, v89, vcc
	v_cmp_gt_u32_e32 vcc, 2.0, v114
	v_sub_u32_e32 v114, v188, v18
	s_nop 0
	v_cndmask_b32_e32 v90, v181, v90, vcc
	v_cmp_gt_u32_e32 vcc, 2.0, v114
	v_sub_u32_e32 v114, s69, v18
	s_nop 0
	v_cndmask_b32_e32 v91, v181, v91, vcc
	v_cmp_gt_u32_e32 vcc, 2.0, v114
	v_sub_u32_e32 v114, v189, v18
	s_nop 0
	v_cndmask_b32_e32 v92, v181, v92, vcc
	v_cmp_gt_u32_e32 vcc, 2.0, v114
	v_sub_u32_e32 v114, v190, v18
	s_nop 0
	v_cndmask_b32_e32 v93, v181, v93, vcc
	v_cmp_gt_u32_e32 vcc, 2.0, v114
	v_sub_u32_e32 v114, v191, v18
	s_nop 0
	v_cndmask_b32_e32 v94, v181, v94, vcc
	v_cmp_gt_u32_e32 vcc, 2.0, v114
	v_sub_u32_e32 v114, s70, v18
	s_nop 0
	v_cndmask_b32_e32 v95, v181, v95, vcc
	v_cmp_gt_u32_e32 vcc, 2.0, v114
	v_sub_u32_e32 v114, v192, v18
	s_nop 0
	v_cndmask_b32_e32 v96, v181, v96, vcc
	v_cmp_gt_u32_e32 vcc, 2.0, v114
	v_sub_u32_e32 v114, v193, v18
	v_sub_u32_e32 v18, v194, v18
	v_cndmask_b32_e32 v97, v181, v97, vcc
	v_cmp_gt_u32_e32 vcc, 2.0, v114
	s_nop 1
	v_cndmask_b32_e32 v98, v181, v98, vcc
	v_cmp_gt_u32_e32 vcc, 2.0, v18
	s_nop 1
	v_cndmask_b32_e32 v99, v181, v99, vcc
	s_branch .LBB0_1806
; __device__ __forceinline__ float xmax16(float v) { float a = v, b = v; PL_SWAP16(a, b); return fmaxf(a, b); }
; __device__ __forceinline__ float xmax32(float v) { float a = v, b = v; PL_SWAP32(a, b); return fmaxf(a, b); }
; __device__ __forceinline__ void mask_scores(f32x4 (&s)[4], int a, unsigned W, int kb, int q4) {
;     const float NEG = -__builtin_inff();
; #pragma unroll
;     for (int T_ = 0; T_ < 4; ++T_)
; #pragma unroll
;         for (int i = 0; i < 4; ++i) if ((unsigned)(a - (kb + 16 * T_ + 4 * q4 + i)) >= W) s[T_][i] = NEG;
; }
; template <class G> __device__ __forceinline__ void online_sm8(f32x4 (&s)[4], G& g, const float ref) {
;     float mx = s[0][0];
; #pragma unroll
;     for (int T_ = 0; T_ < 4; ++T_)
; #pragma unroll
;         for (int i = 0; i < 4; ++i) mx = fmaxf(mx, s[T_][i]);
;     const float t = mx + (ref - 5.f);
;     if (!__all(t <= g.m + SM_THR8)) {
;         const float mr = xmax32(xmax16(t));
;         const float mn = fmaxf(g.m, mr); const float al = __builtin_amdgcn_exp2f(g.m - mn); g.m = mn; g.l *= al;
; #pragma unroll
;         for (int dt = 0; dt < 8; ++dt) g.o[dt] = g.o[dt] * al;
;         const float d = ref - mn;
; #pragma unroll
;         for (int T_ = 0; T_ < 4; ++T_)
; #pragma unroll
;             for (int i = 0; i < 4; ++i) s[T_][i] += d;
;     }
.Lsel_resc_g0:
	v_mov_b32_e32 v18, v84
	v_mov_b32_e32 v84, v150
	s_nop 1
	v_permlane16_swap_b32 v84, v150
	v_mov_b32_e32 v151, v96
	v_max_f32_e32 v114, v150, v150
	v_max_f32_e32 v84, v84, v84
	v_max_f32_e32 v84, v84, v114
	v_mov_b32_e32 v114, v84
	s_nop 1
	v_permlane32_swap_b32 v114, v84
	v_mov_b32_e32 v150, v92
	v_max3_f32 v114, v19, v114, v84
	v_sub_f32_e32 v19, v19, v114
	v_exp_f32_e32 v84, v19
	v_mov_b32_e32 v19, v88
	v_mov_b32_e32 v210, v85
	v_mov_b32_e32 v211, v86
	v_mul_f32_e32 v183, v183, v84
	v_pk_mul_f32 v[82:83], v[82:83], v[84:85] op_sel_hi:[1,0]
	v_pk_mul_f32 v[80:81], v[80:81], v[84:85] op_sel_hi:[1,0]
	v_pk_mul_f32 v[78:79], v[78:79], v[84:85] op_sel_hi:[1,0]
	v_pk_mul_f32 v[76:77], v[76:77], v[84:85] op_sel_hi:[1,0]
	v_pk_mul_f32 v[74:75], v[74:75], v[84:85] op_sel_hi:[1,0]
	v_pk_mul_f32 v[72:73], v[72:73], v[84:85] op_sel_hi:[1,0]
	v_pk_mul_f32 v[70:71], v[70:71], v[84:85] op_sel_hi:[1,0]
	v_pk_mul_f32 v[68:69], v[68:69], v[84:85] op_sel_hi:[1,0]
	v_pk_mul_f32 v[66:67], v[66:67], v[84:85] op_sel_hi:[1,0]
	v_pk_mul_f32 v[64:65], v[64:65], v[84:85] op_sel_hi:[1,0]
	v_pk_mul_f32 v[62:63], v[62:63], v[84:85] op_sel_hi:[1,0]
	v_pk_mul_f32 v[60:61], v[60:61], v[84:85] op_sel_hi:[1,0]
	v_pk_mul_f32 v[58:59], v[58:59], v[84:85] op_sel_hi:[1,0]
	v_pk_mul_f32 v[56:57], v[56:57], v[84:85] op_sel_hi:[1,0]
	v_pk_mul_f32 v[54:55], v[54:55], v[84:85] op_sel_hi:[1,0]
	v_pk_mul_f32 v[52:53], v[52:53], v[84:85] op_sel_hi:[1,0]
	v_sub_f32_e32 v84, v219, v114
	v_pk_add_f32 v[212:213], v[18:19], v[84:85] op_sel_hi:[1,0]
	v_mov_b32_e32 v18, v89
	v_mov_b32_e32 v19, v90
	v_pk_add_f32 v[214:215], v[18:19], v[84:85] op_sel_hi:[1,0]
	v_mov_b32_e32 v18, v93
	v_mov_b32_e32 v19, v94
	v_pk_add_f32 v[88:89], v[18:19], v[84:85] op_sel_hi:[1,0]
	v_mov_b32_e32 v18, v97
	v_mov_b32_e32 v19, v98
	v_pk_add_f32 v[210:211], v[210:211], v[84:85] op_sel_hi:[1,0]
	v_pk_add_f32 v[150:151], v[150:151], v[84:85] op_sel_hi:[1,0]
	v_pk_add_f32 v[92:93], v[18:19], v[84:85] op_sel_hi:[1,0]
	v_add_f32_e32 v87, v87, v84
	v_add_f32_e32 v91, v91, v84
	v_add_f32_e32 v95, v95, v84
	v_add_f32_e32 v99, v99, v84
	v_mov_b32_e32 v19, v114
	v_cmp_ngt_f32_e32 vcc, s90, v19
	v_mov_b32_e32 v97, v92
	v_mov_b32_e32 v98, v93
	v_mov_b32_e32 v93, v88
	v_mov_b32_e32 v94, v89
	v_mov_b32_e32 v89, v214
	v_mov_b32_e32 v90, v215
	v_mov_b32_e32 v85, v210
	v_mov_b32_e32 v86, v211
	v_mov_b32_e32 v84, v212
	v_mov_b32_e32 v88, v213
	v_mov_b32_e32 v92, v150
	v_mov_b32_e32 v96, v151
	v_cndmask_b32_e32 v219, 0, v19, vcc
	v_add_f32_e32 v218, v19, v115
	v_sub_f32_e32 v216, 0x40a00000, v219
	v_add_f32_e32 v217, 0xc0a00000, v219
	s_branch .LBB0_1808
.Lsel_diag_g1:
	s_lshl_b32 s12, s44, 6
	v_add_u32_e32 v114, s12, v155
	v_sub_u32_e32 v116, v195, v114
	v_cmp_gt_u32_e32 vcc, 2.0, v116
	v_sub_u32_e32 v116, v114, v195
	s_nop 2
	v_cndmask_b32_e32 v84, v181, v84, vcc
	v_cmp_lt_u32_e32 vcc, s91, v116
	v_sub_u32_e32 v116, v196, v114
	s_nop 0
	v_cndmask_b32_e32 v85, v181, v85, vcc
	v_cmp_gt_u32_e32 vcc, 2.0, v116
	v_sub_u32_e32 v116, v197, v114
	s_nop 0
	v_cndmask_b32_e32 v86, v181, v86, vcc
	v_cmp_gt_u32_e32 vcc, 2.0, v116
	v_sub_u32_e32 v116, s71, v114
	s_nop 0
	v_cndmask_b32_e32 v87, v181, v87, vcc
	v_cmp_gt_u32_e32 vcc, 2.0, v116
	v_sub_u32_e32 v116, v198, v114
	s_nop 0
	v_cndmask_b32_e32 v88, v181, v88, vcc
	v_cmp_gt_u32_e32 vcc, 2.0, v116
	v_sub_u32_e32 v116, v199, v114
	s_nop 0
	v_cndmask_b32_e32 v89, v181, v89, vcc
	v_cmp_gt_u32_e32 vcc, 2.0, v116
	v_sub_u32_e32 v116, v200, v114
	s_nop 0
	v_cndmask_b32_e32 v90, v181, v90, vcc
	v_cmp_gt_u32_e32 vcc, 2.0, v116
	v_sub_u32_e32 v116, s72, v114
	s_nop 0
	v_cndmask_b32_e32 v91, v181, v91, vcc
	v_cmp_gt_u32_e32 vcc, 2.0, v116
	v_sub_u32_e32 v116, v201, v114
	s_nop 0
	v_cndmask_b32_e32 v92, v181, v92, vcc
	v_cmp_gt_u32_e32 vcc, 2.0, v116
	v_sub_u32_e32 v116, v202, v114
	s_nop 0
	v_cndmask_b32_e32 v93, v181, v93, vcc
	v_cmp_gt_u32_e32 vcc, 2.0, v116
	v_sub_u32_e32 v116, v203, v114
	s_nop 0
	v_cndmask_b32_e32 v94, v181, v94, vcc
	v_cmp_gt_u32_e32 vcc, 2.0, v116
	v_sub_u32_e32 v116, s73, v114
	s_nop 0
	v_cndmask_b32_e32 v95, v181, v95, vcc
	v_cmp_gt_u32_e32 vcc, 2.0, v116
	v_sub_u32_e32 v116, v204, v114
	s_nop 0
	v_cndmask_b32_e32 v96, v181, v96, vcc
	v_cmp_gt_u32_e32 vcc, 2.0, v116
	v_sub_u32_e32 v116, v205, v114
	v_sub_u32_e32 v114, v206, v114
	v_cndmask_b32_e32 v97, v181, v97, vcc
	v_cmp_gt_u32_e32 vcc, 2.0, v116
	s_nop 1
	v_cndmask_b32_e32 v98, v181, v98, vcc
	v_cmp_gt_u32_e32 vcc, 2.0, v114
	s_nop 1
	v_cndmask_b32_e32 v99, v181, v99, vcc
	s_branch .LBB0_1812
; __device__ __forceinline__ float xmax16(float v) { float a = v, b = v; PL_SWAP16(a, b); return fmaxf(a, b); }
; __device__ __forceinline__ float xmax32(float v) { float a = v, b = v; PL_SWAP32(a, b); return fmaxf(a, b); }
; template <class G> __device__ __forceinline__ void online_sm8(f32x4 (&s)[4], G& g, const float ref) {
;     float mx = s[0][0];
; #pragma unroll
;     for (int T_ = 0; T_ < 4; ++T_)
; #pragma unroll
;         for (int i = 0; i < 4; ++i) mx = fmaxf(mx, s[T_][i]);
;     const float t = mx + (ref - 5.f);
;     if (!__all(t <= g.m + SM_THR8)) {
;         const float mr = xmax32(xmax16(t));
;         const float mn = fmaxf(g.m, mr); const float al = __builtin_amdgcn_exp2f(g.m - mn); g.m = mn; g.l *= al;
; #pragma unroll
;         for (int dt = 0; dt < 8; ++dt) g.o[dt] = g.o[dt] * al;
;         const float d = ref - mn;
; #pragma unroll
;         for (int T_ = 0; T_ < 4; ++T_)
; #pragma unroll
;             for (int i = 0; i < 4; ++i) s[T_][i] += d;
;     }
.Lsel_resc_g1:
	v_mov_b32_e32 v116, v84
	v_mov_b32_e32 v84, v150
	s_nop 1
	v_permlane16_swap_b32 v150, v84
	v_mov_b32_e32 v151, v96
	v_max_f32_e32 v84, v84, v84
	v_max_f32_e32 v114, v150, v150
	v_max_f32_e32 v84, v114, v84
	v_mov_b32_e32 v114, v84
	s_nop 1
	v_permlane32_swap_b32 v84, v114
	v_mov_b32_e32 v150, v92
	v_max3_f32 v114, v117, v84, v114
	v_sub_f32_e32 v84, v117, v114
	v_exp_f32_e32 v84, v84
	v_sub_f32_e32 v18, v223, v114
	v_mov_b32_e32 v117, v88
	v_mov_b32_e32 v88, v93
	v_mul_f32_e32 v182, v182, v84
	v_pk_mul_f32 v[50:51], v[50:51], v[84:85] op_sel_hi:[1,0]
	v_pk_mul_f32 v[48:49], v[48:49], v[84:85] op_sel_hi:[1,0]
	v_pk_mul_f32 v[46:47], v[46:47], v[84:85] op_sel_hi:[1,0]
	v_pk_mul_f32 v[44:45], v[44:45], v[84:85] op_sel_hi:[1,0]
	v_pk_mul_f32 v[42:43], v[42:43], v[84:85] op_sel_hi:[1,0]
	v_pk_mul_f32 v[40:41], v[40:41], v[84:85] op_sel_hi:[1,0]
	v_pk_mul_f32 v[38:39], v[38:39], v[84:85] op_sel_hi:[1,0]
	v_pk_mul_f32 v[36:37], v[36:37], v[84:85] op_sel_hi:[1,0]
	v_pk_mul_f32 v[34:35], v[34:35], v[84:85] op_sel_hi:[1,0]
	v_pk_mul_f32 v[32:33], v[32:33], v[84:85] op_sel_hi:[1,0]
	v_pk_mul_f32 v[30:31], v[30:31], v[84:85] op_sel_hi:[1,0]
	v_pk_mul_f32 v[28:29], v[28:29], v[84:85] op_sel_hi:[1,0]
	v_pk_mul_f32 v[26:27], v[26:27], v[84:85] op_sel_hi:[1,0]
	v_pk_mul_f32 v[24:25], v[24:25], v[84:85] op_sel_hi:[1,0]
	v_pk_mul_f32 v[22:23], v[22:23], v[84:85] op_sel_hi:[1,0]
	v_pk_mul_f32 v[20:21], v[20:21], v[84:85] op_sel_hi:[1,0]
	v_mov_b32_e32 v84, v85
	v_mov_b32_e32 v85, v86
	v_pk_add_f32 v[210:211], v[84:85], v[18:19] op_sel_hi:[1,0]
	v_mov_b32_e32 v84, v89
	v_mov_b32_e32 v85, v90
	v_mov_b32_e32 v89, v94
	v_mov_b32_e32 v92, v97
	v_mov_b32_e32 v93, v98
	v_pk_add_f32 v[212:213], v[116:117], v[18:19] op_sel_hi:[1,0]
	v_pk_add_f32 v[84:85], v[84:85], v[18:19] op_sel_hi:[1,0]
	v_pk_add_f32 v[88:89], v[88:89], v[18:19] op_sel_hi:[1,0]
	v_pk_add_f32 v[150:151], v[150:151], v[18:19] op_sel_hi:[1,0]
	v_pk_add_f32 v[92:93], v[92:93], v[18:19] op_sel_hi:[1,0]
	v_add_f32_e32 v87, v87, v18
	v_add_f32_e32 v91, v91, v18
	v_add_f32_e32 v95, v95, v18
	v_add_f32_e32 v99, v99, v18
	v_mov_b32_e32 v117, v114
	v_cmp_ngt_f32_e32 vcc, s90, v117
	v_mov_b32_e32 v97, v92
	v_mov_b32_e32 v98, v93
	v_mov_b32_e32 v93, v88
	v_mov_b32_e32 v94, v89
	v_mov_b32_e32 v89, v84
	v_mov_b32_e32 v90, v85
	v_mov_b32_e32 v85, v210
	v_mov_b32_e32 v86, v211
	v_mov_b32_e32 v84, v212
	v_mov_b32_e32 v88, v213
	v_mov_b32_e32 v92, v150
	v_mov_b32_e32 v96, v151
	v_cndmask_b32_e32 v223, 0, v117, vcc
	v_add_f32_e32 v222, v117, v115
	v_sub_f32_e32 v220, 0x40a00000, v223
	v_add_f32_e32 v221, 0xc0a00000, v223
	s_branch .LBB0_1797
